# grid barrier: acquire invalidate issued with the arrival atomic; completing leader releases all XCD generation words directly
# speedup vs baseline: 1.0112x; 1.0112x over previous
.LBB0_148:
	s_lshl_b32 s0, s27, 8
	s_add_u32 s4, s16, s0
	s_addc_u32 s5, s17, 0
	v_mov_b32_e32 v2, 0x1000
	v_mov_b32_e32 v4, 1
	global_atomic_add v4, v2, v4, s[4:5] offset:1024 sc0
	buffer_inv sc1
	v_cvt_f32_u32_e32 v2, v3
	v_sub_u32_e32 v5, 0, v3
	v_rcp_iflag_f32_e32 v2, v2
	s_nop 0
	v_mul_f32_e32 v2, 0x4f7ffffe, v2
	v_cvt_u32_f32_e32 v2, v2
	v_mul_lo_u32 v5, v5, v2
	v_mul_hi_u32 v5, v2, v5
	v_add_u32_e32 v2, v2, v5
	s_waitcnt vmcnt(0)
	v_mul_hi_u32 v2, v4, v2
	v_mul_lo_u32 v5, v2, v3
	v_sub_u32_e32 v5, v4, v5
	v_add_u32_e32 v6, 1, v2
	v_cmp_ge_u32_e32 vcc, v5, v3
	v_add_u32_e32 v4, 1, v4
	s_nop 0
	v_cndmask_b32_e32 v2, v2, v6, vcc
	v_sub_u32_e32 v6, v5, v3
	v_cndmask_b32_e32 v5, v5, v6, vcc
	v_add_u32_e32 v6, 1, v2
	v_cmp_ge_u32_e32 vcc, v5, v3
	s_nop 1
	v_cndmask_b32_e32 v2, v2, v6, vcc
	v_mul_lo_u32 v5, v3, v2
	v_add_u32_e32 v3, v5, v3
	v_cmp_ne_u32_e32 vcc, v4, v3
	s_and_saveexec_b64 s[0:1], vcc
	s_xor_b64 s[0:1], exec, s[0:1]
	s_cbranch_execz .LBB0_162
	s_waitcnt lgkmcnt(0)
	v_mov_b32_e32 v1, 0x2000
	global_load_dword v1, v1, s[4:5] offset:1024 sc1
	s_add_u32 s10, s4, 0x2400
	s_addc_u32 s11, s5, 0
	s_waitcnt vmcnt(0)
	v_cmp_eq_u32_e32 vcc, v1, v2
	s_and_saveexec_b64 s[6:7], vcc
	s_cbranch_execz .LBB0_161
	v_readlane_b32 s8, v254, 2
	v_readlane_b32 s9, v254, 3
	s_add_u32 s8, s8, 0x4200
	s_addc_u32 s9, s9, 0
	s_mov_b32 s24, 1
	s_mov_b64 s[12:13], 0
	v_mov_b32_e32 v1, 0
	s_branch .LBB0_152

.LBB0_161:
	s_or_b64 exec, exec, s[6:7]
	s_waitcnt vmcnt(0)
	s_waitcnt vmcnt(0)

.LBB0_182:
	s_or_b64 exec, exec, s[0:1]
	v_readlane_b32 s0, v254, 59
	v_readlane_b32 s1, v254, 60
	s_waitcnt vmcnt(0)
	buffer_inv sc1
	s_nop 2
	s_waitcnt vmcnt(0)

.LBB0_257:
	v_readlane_b32 s0, v254, 57
	v_readlane_b32 s1, v254, 58
	v_cvt_f32_u32_e32 v1, v3
	v_sub_u32_e32 v5, 0, v3
	v_rcp_iflag_f32_e32 v1, v1
	s_nop 1
	global_atomic_add v4, v34, v235, s[0:1] sc0
	buffer_inv sc1
	v_mul_f32_e32 v1, 0x4f7ffffe, v1
	v_cvt_u32_f32_e32 v1, v1
	v_mul_lo_u32 v5, v5, v1
	v_mul_hi_u32 v5, v1, v5
	v_add_u32_e32 v1, v1, v5
	s_waitcnt vmcnt(0)
	v_mul_hi_u32 v1, v4, v1
	v_mul_lo_u32 v5, v1, v3
	v_sub_u32_e32 v5, v4, v5
	v_add_u32_e32 v6, 1, v1
	v_cmp_ge_u32_e32 vcc, v5, v3
	v_add_u32_e32 v4, 1, v4
	s_nop 0
	v_cndmask_b32_e32 v1, v1, v6, vcc
	v_sub_u32_e32 v6, v5, v3
	v_cndmask_b32_e32 v5, v5, v6, vcc
	v_add_u32_e32 v6, 1, v1
	v_cmp_ge_u32_e32 vcc, v5, v3
	s_nop 1
	v_cndmask_b32_e32 v1, v1, v6, vcc
	v_mul_lo_u32 v5, v3, v1
	v_add_u32_e32 v3, v5, v3
	v_cmp_ne_u32_e32 vcc, v4, v3
	s_and_saveexec_b64 s[0:1], vcc
	s_xor_b64 s[0:1], exec, s[0:1]
	s_cbranch_execz .LBB0_271
	v_readlane_b32 s14, v254, 59
	v_readlane_b32 s15, v254, 60
	s_waitcnt lgkmcnt(0)
	s_nop 3
	global_load_dword v2, v34, s[14:15] sc1
	s_waitcnt vmcnt(0)
	v_cmp_eq_u32_e32 vcc, v2, v1
	s_and_saveexec_b64 s[14:15], vcc
	s_cbranch_execz .LBB0_270
	s_mov_b32 s40, 1
	s_mov_b64 s[16:17], 0
	s_branch .LBB0_261

.LBB0_270:
	s_or_b64 exec, exec, s[14:15]
	s_waitcnt vmcnt(0)
	s_waitcnt vmcnt(0)

.LBB0_286:
	s_or_b64 exec, exec, s[0:1]
	s_and_saveexec_b64 s[0:1], s[14:15]
	s_cbranch_execz .LBB0_288
	global_atomic_add v[2:3], v235, off
	v_add_co_u32_e32 v2, vcc, 0xffffef00, v2
	s_nop 1
	v_addc_co_u32_e32 v3, vcc, -1, v3, vcc
	global_atomic_add v[2:3], v235, off
	global_atomic_add v[2:3], v235, off offset:256
	global_atomic_add v[2:3], v235, off offset:512
	global_atomic_add v[2:3], v235, off offset:768
	global_atomic_add v[2:3], v235, off offset:1024
	global_atomic_add v[2:3], v235, off offset:1280
	global_atomic_add v[2:3], v235, off offset:1536
	global_atomic_add v[2:3], v235, off offset:1792
	global_atomic_add v[2:3], v235, off offset:2048
	global_atomic_add v[2:3], v235, off offset:2304
	global_atomic_add v[2:3], v235, off offset:2560
	global_atomic_add v[2:3], v235, off offset:2816
	global_atomic_add v[2:3], v235, off offset:3072
	global_atomic_add v[2:3], v235, off offset:3328
	global_atomic_add v[2:3], v235, off offset:3584
	global_atomic_add v[2:3], v235, off offset:3840

.LBB0_468:
	v_ashrrev_i32_e32 v31, 31, v30
	v_lshlrev_b64 v[30:31], 9, v[30:31]
	v_lshl_add_u64 v[40:41], v[84:85], 0, v[30:31]
	ds_read_b128 v[30:33], v96 offset:48384
	ds_read_b128 v[42:45], v96 offset:48400
	s_add_i32 s91, s91, 64
	s_sub_i32 s89, s89, 64
	s_add_i32 s92, s92, 1
	s_waitcnt lgkmcnt(1)
	v_lshlrev_b32_e32 v35, 16, v30
	v_and_b32_e32 v30, 0xffff0000, v30
	v_mul_f32_e32 v35, 4.0, v35
	v_mul_f32_e32 v30, 4.0, v30
	v_med3_f32 v35, v35, s75, v238
	v_med3_f32 v47, v30, s75, v238
	v_mov_b32_e32 v30, 0
	v_cvt_pk_fp8_f32 v30, v35, v47
	v_lshlrev_b32_e32 v46, 16, v31
	v_and_b32_e32 v31, 0xffff0000, v31
	v_mul_f32_e32 v46, 4.0, v46
	v_mul_f32_e32 v31, 4.0, v31
	v_med3_f32 v46, v46, s75, v238
	v_med3_f32 v31, v31, s75, v238
	v_cvt_pk_fp8_f32 v30, v46, v31 op_sel:[0,0,1]
	v_lshlrev_b32_e32 v31, 16, v32
	v_and_b32_e32 v32, 0xffff0000, v32
	v_mul_f32_e32 v31, 4.0, v31
	v_mul_f32_e32 v32, 4.0, v32
	v_med3_f32 v46, v31, s75, v238
	v_med3_f32 v32, v32, s75, v238
	v_mov_b32_e32 v31, 0
	v_cvt_pk_fp8_f32 v31, v46, v32
	v_lshlrev_b32_e32 v35, 16, v33
	v_and_b32_e32 v33, 0xffff0000, v33
	v_mul_f32_e32 v35, 4.0, v35
	v_mul_f32_e32 v33, 4.0, v33
	v_med3_f32 v35, v35, s75, v238
	v_med3_f32 v33, v33, s75, v238
	v_cvt_pk_fp8_f32 v31, v35, v33 op_sel:[0,0,1]
	s_waitcnt lgkmcnt(0)
	v_lshlrev_b32_e32 v32, 16, v42
	v_and_b32_e32 v33, 0xffff0000, v42
	v_mul_f32_e32 v32, 4.0, v32
	v_mul_f32_e32 v33, 4.0, v33
	v_lshlrev_b32_e32 v35, 16, v43
	v_and_b32_e32 v42, 0xffff0000, v43
	v_med3_f32 v43, v32, s75, v238
	v_med3_f32 v33, v33, s75, v238
	v_mov_b32_e32 v32, 0
	v_cvt_pk_fp8_f32 v32, v43, v33
	v_mul_f32_e32 v35, 4.0, v35
	v_mul_f32_e32 v42, 4.0, v42
	v_med3_f32 v35, v35, s75, v238
	v_med3_f32 v42, v42, s75, v238
	v_cvt_pk_fp8_f32 v32, v35, v42 op_sel:[0,0,1]
	v_lshlrev_b32_e32 v33, 16, v44
	v_and_b32_e32 v35, 0xffff0000, v44
	v_mul_f32_e32 v33, 4.0, v33
	v_mul_f32_e32 v35, 4.0, v35
	v_med3_f32 v44, v33, s75, v238
	v_med3_f32 v35, v35, s75, v238
	v_mov_b32_e32 v33, 0
	v_cvt_pk_fp8_f32 v33, v44, v35
	v_lshlrev_b32_e32 v42, 16, v45
	v_and_b32_e32 v43, 0xffff0000, v45
	v_mul_f32_e32 v42, 4.0, v42
	v_mul_f32_e32 v43, 4.0, v43
	v_med3_f32 v42, v42, s75, v238
	v_med3_f32 v43, v43, s75, v238
	v_cvt_pk_fp8_f32 v33, v42, v43 op_sel:[0,0,1]
	s_cmpk_eq_i32 s91, 0x900
	global_store_dwordx4 v[40:41], v[30:33], off
	s_waitcnt vmcnt(38)
	s_waitcnt vmcnt(35)
	s_waitcnt vmcnt(32)
	s_waitcnt vmcnt(29)
	s_waitcnt vmcnt(26)
	s_waitcnt vmcnt(23)
	s_waitcnt vmcnt(20)
	s_waitcnt vmcnt(17)
	s_waitcnt vmcnt(16)
	s_waitcnt vmcnt(15)
	s_waitcnt vmcnt(14)
	s_waitcnt vmcnt(13)
	s_waitcnt vmcnt(12)
	s_waitcnt vmcnt(11)
	s_waitcnt vmcnt(10)
	s_waitcnt vmcnt(9)
	s_waitcnt vmcnt(8)
	s_waitcnt vmcnt(7)
	s_waitcnt vmcnt(6)
	s_waitcnt vmcnt(5)
	s_waitcnt vmcnt(4)
	s_waitcnt vmcnt(3)
	s_waitcnt vmcnt(2)
	s_waitcnt vmcnt(1)
	s_cbranch_scc1 .LBB0_466
.LBB0_469:
	v_lshlrev_b32_e32 v30, 16, v117
	v_add_f32_e32 v32, 0, v30
	v_lshlrev_b32_e32 v30, 16, v120
	v_add_f32_e32 v40, v32, v30
	v_lshlrev_b32_e32 v30, 16, v123
	v_add_f32_e32 v41, v40, v30
	v_lshlrev_b32_e32 v30, 16, v128
	v_add_f32_e32 v42, v41, v30
	v_lshlrev_b32_e32 v30, 16, v131
	v_add_f32_e32 v43, v42, v30
	v_lshlrev_b32_e32 v30, 16, v134
	v_add_f32_e32 v44, v43, v30
	v_lshlrev_b32_e32 v30, 16, v137
	v_add_f32_e32 v45, v44, v30
	v_lshlrev_b32_e32 v30, 16, v140
	v_add_f32_e32 v33, v45, v30
	v_add_u32_e32 v30, s86, v91
	ds_write_b32 v30, v33 offset:46080
	s_waitcnt lgkmcnt(0)
	s_barrier
	ds_read2st64_b32 v[30:31], v91 offset0:180 offset1:181
	v_lshlrev_b32_e32 v47, 16, v115
	v_mul_f32_e32 v47, 0x3e000000, v47
	v_lshlrev_b32_e32 v48, 16, v116
	s_andn2_b64 vcc, exec, s[18:19]
	s_waitcnt lgkmcnt(0)
	v_add_f32_e32 v30, 0, v30
	v_cndmask_b32_e64 v35, 0, v30, s[42:43]
	v_add_f32_e32 v46, v30, v31
	v_add_f32_e32 v30, v31, v35
	v_cndmask_b32_e64 v35, v35, v30, s[44:45]
	ds_read2st64_b32 v[30:31], v91 offset0:182 offset1:183
	s_waitcnt lgkmcnt(0)
	v_add_f32_e32 v46, v46, v30
	v_add_f32_e32 v30, v30, v35
	v_cndmask_b32_e64 v30, v35, v30, s[46:47]
	v_add_f32_e32 v35, v46, v31
	v_add_f32_e32 v31, v31, v30
	v_cndmask_b32_e64 v46, v30, v31, s[48:49]
	ds_read2st64_b32 v[30:31], v91 offset0:184 offset1:185
	s_waitcnt lgkmcnt(0)
	v_add_f32_e32 v35, v35, v30
	v_add_f32_e32 v30, v30, v46
	v_cndmask_b32_e64 v30, v46, v30, s[50:51]
	v_add_f32_e32 v35, v35, v31
	v_add_f32_e32 v31, v31, v30
	v_cndmask_b32_e64 v46, v30, v31, s[52:53]
	ds_read2st64_b32 v[30:31], v91 offset0:186 offset1:187
	s_waitcnt lgkmcnt(0)
	v_add_f32_e32 v35, v35, v30
	v_add_f32_e32 v30, v30, v46
	v_cndmask_b32_e64 v30, v46, v30, s[54:55]
	v_add_f32_e32 v35, v35, v31
	v_add_f32_e32 v31, v31, v30
	v_cndmask_b32_e64 v46, v30, v31, s[56:57]
	v_mul_f32_e32 v30, 0x3fb8aa3b, v35
	v_exp_f32_e32 v35, v30
	v_add_f32_e32 v30, v32, v46
	v_mul_f32_e32 v30, 0x3fb8aa3b, v30
	v_exp_f32_e32 v30, v30
	v_add_f32_e32 v33, v33, v46
	v_mul_f32_e32 v33, 0x3fb8aa3b, v33
	v_exp_f32_e32 v33, v33
	v_rcp_f32_e32 v31, v30
	v_mul_f32_e32 v30, v47, v30
	v_cvt_pk_bf16_f32 v30, v30, s0
	s_mul_i32 s0, s71, 0x480
	v_add_u32_e32 v47, s0, v92
	v_mul_f32_e32 v32, v35, v31
	ds_write_b16 v47, v30
	v_mul_f32_e32 v30, v31, v48
	v_add_f32_e32 v31, v40, v46
	v_mul_f32_e32 v31, 0x3fb8aa3b, v31
	v_exp_f32_e32 v31, v31
	v_cvt_pk_bf16_f32 v30, v30, s0
	ds_write_b16 v47, v30 offset:9216
	v_mul_f32_e32 v30, v32, v48
	v_rcp_f32_e32 v32, v31
	v_lshlrev_b32_e32 v40, 16, v118
	v_mul_f32_e32 v40, 0x3e000000, v40
	v_mul_f32_e32 v31, v40, v31
	v_lshlrev_b32_e32 v48, 16, v119
	v_cvt_pk_bf16_f32 v31, v31, s0
	ds_write_b16 v47, v31 offset:144
	v_mul_f32_e32 v31, v32, v48
	v_cvt_pk_bf16_f32 v31, v31, s0
	ds_write_b16 v47, v31 offset:9360
	v_mul_f32_e32 v31, v35, v32
	v_mul_f32_e32 v31, v31, v48
	v_cvt_pk_bf16_f32 v31, v31, 0
	v_cvt_pk_bf16_f32 v30, v30, 0
	v_lshlrev_b32_e32 v31, 16, v31
	v_and_or_b32 v30, v30, s27, v31
	v_add_f32_e32 v31, v41, v46
	v_mul_f32_e32 v31, 0x3fb8aa3b, v31
	v_exp_f32_e32 v31, v31
	v_lshlrev_b32_e32 v41, 16, v121
	v_mul_f32_e32 v41, 0x3e000000, v41
	v_lshlrev_b32_e32 v48, 16, v122
	v_rcp_f32_e32 v32, v31
	v_mul_f32_e32 v31, v41, v31
	v_cvt_pk_bf16_f32 v31, v31, s0
	ds_write_b16 v47, v31 offset:288
	v_mul_f32_e32 v40, v35, v32
	v_mul_f32_e32 v31, v32, v48
	v_add_f32_e32 v32, v42, v46
	v_mul_f32_e32 v32, 0x3fb8aa3b, v32
	v_exp_f32_e32 v32, v32
	v_cvt_pk_bf16_f32 v31, v31, s0
	ds_write_b16 v47, v31 offset:9504
	v_mul_f32_e32 v31, v40, v48
	v_rcp_f32_e32 v40, v32
	v_lshlrev_b32_e32 v41, 16, v124
	v_mul_f32_e32 v41, 0x3e000000, v41
	v_mul_f32_e32 v32, v41, v32
	v_lshlrev_b32_e32 v42, 16, v125
	v_cvt_pk_bf16_f32 v32, v32, s0
	ds_write_b16 v47, v32 offset:432
	v_mul_f32_e32 v32, v40, v42
	v_cvt_pk_bf16_f32 v32, v32, s0
	ds_write_b16 v47, v32 offset:9648
	v_mul_f32_e32 v32, v35, v40
	v_mul_f32_e32 v32, v32, v42
	v_cvt_pk_bf16_f32 v32, v32, 0
	v_cvt_pk_bf16_f32 v31, v31, 0
	v_lshlrev_b32_e32 v32, 16, v32
	v_and_or_b32 v31, v31, s27, v32
	v_add_f32_e32 v32, v43, v46
	v_mul_f32_e32 v32, 0x3fb8aa3b, v32
	v_exp_f32_e32 v32, v32
	v_lshlrev_b32_e32 v42, 16, v129
	v_mul_f32_e32 v42, 0x3e000000, v42
	v_lshlrev_b32_e32 v43, 16, v130
	v_rcp_f32_e32 v40, v32
	v_mul_f32_e32 v32, v42, v32
	v_cvt_pk_bf16_f32 v32, v32, s0
	ds_write_b16 v47, v32 offset:576
	v_mul_f32_e32 v41, v35, v40
	v_mul_f32_e32 v32, v40, v43
	v_add_f32_e32 v40, v44, v46
	v_mul_f32_e32 v40, 0x3fb8aa3b, v40
	v_exp_f32_e32 v40, v40
	v_cvt_pk_bf16_f32 v32, v32, s0
	ds_write_b16 v47, v32 offset:9792
	v_mul_f32_e32 v32, v41, v43
	v_rcp_f32_e32 v41, v40
	v_lshlrev_b32_e32 v42, 16, v132
	v_mul_f32_e32 v42, 0x3e000000, v42
	v_mul_f32_e32 v40, v42, v40
	v_lshlrev_b32_e32 v43, 16, v133
	v_cvt_pk_bf16_f32 v40, v40, s0
	ds_write_b16 v47, v40 offset:720
	v_mul_f32_e32 v40, v41, v43
	v_cvt_pk_bf16_f32 v40, v40, s0
	ds_write_b16 v47, v40 offset:9936
	v_mul_f32_e32 v40, v35, v41
	v_mul_f32_e32 v40, v40, v43
	v_cvt_pk_bf16_f32 v40, v40, 0
	v_cvt_pk_bf16_f32 v32, v32, 0
	v_lshlrev_b32_e32 v40, 16, v40
	v_and_or_b32 v32, v32, s27, v40
	v_add_f32_e32 v40, v45, v46
	v_mul_f32_e32 v40, 0x3fb8aa3b, v40
	v_exp_f32_e32 v40, v40
	v_lshlrev_b32_e32 v43, 16, v135
	v_mul_f32_e32 v43, 0x3e000000, v43
	v_lshlrev_b32_e32 v44, 16, v136
	v_rcp_f32_e32 v41, v40
	v_mul_f32_e32 v40, v43, v40
	v_cvt_pk_bf16_f32 v40, v40, s0
	ds_write_b16 v47, v40 offset:864
	v_mul_f32_e32 v40, v41, v44
	v_mul_f32_e32 v42, v35, v41
	v_cvt_pk_bf16_f32 v40, v40, s0
	ds_write_b16 v47, v40 offset:10080
	v_mul_f32_e32 v40, v42, v44
	v_rcp_f32_e32 v41, v33
	v_lshlrev_b32_e32 v42, 16, v138
	v_mul_f32_e32 v42, 0x3e000000, v42
	v_mul_f32_e32 v33, v42, v33
	v_lshlrev_b32_e32 v43, 16, v139
	v_cvt_pk_bf16_f32 v33, v33, s0
	ds_write_b16 v47, v33 offset:1008
	v_mul_f32_e32 v33, v41, v43
	v_cvt_pk_bf16_f32 v33, v33, s0
	ds_write_b16 v47, v33 offset:10224
	v_mul_f32_e32 v33, v35, v41
	v_mul_f32_e32 v33, v33, v43
	v_cvt_pk_bf16_f32 v33, v33, 0
	v_cvt_pk_bf16_f32 v40, v40, 0
	v_lshlrev_b32_e32 v33, 16, v33
	v_and_or_b32 v33, v40, s27, v33
	v_add_u32_e32 v40, s87, v93
	ds_write_b128 v40, v[30:33] offset:18432
	s_cbranch_vccnz .LBB0_471
	ds_write_b32 v109, v35 offset:48128
.LBB0_471:
	v_lshl_or_b32 v30, v1, 16, v2
	v_lshl_or_b32 v31, v3, 16, v4
	v_lshl_or_b32 v32, v5, 16, v6
	v_lshl_or_b32 v33, v7, 16, v8
	ds_write_b128 v94, v[30:33] offset:27648
	v_lshl_or_b32 v30, v9, 16, v10
	v_lshl_or_b32 v31, v11, 16, v12
	v_lshl_or_b32 v32, v13, 16, v14
	v_lshl_or_b32 v33, v15, 16, v16
	s_cmpk_eq_i32 s91, 0x8c0
	ds_write_b128 v94, v[30:33] offset:27664
	s_cbranch_scc1 .LBB0_486
	s_cmp_gt_u32 s92, 2
	s_cselect_b64 s[0:1], -1, 0
	s_mov_b64 s[36:37], -1
	s_and_b64 vcc, exec, s[0:1]
	s_cbranch_vccnz .LBB0_490
	s_andn2_b64 vcc, exec, s[36:37]
	s_cbranch_vccz .LBB0_491

.LBB0_477:
	s_mov_b64 s[64:65], -1
	s_and_b64 vcc, exec, s[0:1]
	v_add_u32_e32 v1, s91, v87
	v_add_u32_e32 v2, s89, v108
	s_cbranch_vccz .LBB0_479
	v_add_u32_e32 v3, 0xffffff40, v1
	v_add_u32_e32 v4, 0x8bf, v2
	v_cndmask_b32_e64 v3, v4, v3, s[58:59]
	v_lshlrev_b32_e32 v4, 6, v3
	v_and_b32_e32 v4, 0x7c0, v4
	v_ashrrev_i32_e32 v5, 5, v3
	v_add_u32_e32 v4, v4, v5
	v_cndmask_b32_e64 v3, v4, v3, s[38:39]
	v_add_u32_e32 v3, s90, v3
	s_mov_b64 s[64:65], 0
.LBB0_479:
	s_andn2_b64 vcc, exec, s[64:65]
	s_cbranch_vccnz .LBB0_481
	v_add3_u32 v3, v87, s91, 64
	v_add_u32_e32 v4, 0xbf, v2
	v_cndmask_b32_e64 v3, v4, v3, s[58:59]
	v_add_u32_e32 v3, s88, v3
.LBB0_481:
	s_nop 0
	v_readfirstlane_b32 s93, v3
	s_mov_b64 s[64:65], -1
	s_and_b64 vcc, exec, s[0:1]
	s_cbranch_vccz .LBB0_483
	v_add_u32_e32 v3, 0xffffff41, v1
	v_add_u32_e32 v4, 0x8be, v2
	v_cndmask_b32_e64 v3, v4, v3, s[58:59]
	v_lshlrev_b32_e32 v4, 6, v3
	v_and_b32_e32 v4, 0x7c0, v4
	v_ashrrev_i32_e32 v5, 5, v3
	v_add_u32_e32 v4, v4, v5
	v_cndmask_b32_e64 v3, v4, v3, s[38:39]
	v_add_u32_e32 v3, s90, v3
	s_mov_b64 s[64:65], 0
.LBB0_483:
	s_andn2_b64 vcc, exec, s[64:65]
	s_cbranch_vccnz .LBB0_485
	v_add_u32_e32 v1, 0x41, v1
	v_add_u32_e32 v2, 0xbe, v2
	v_cndmask_b32_e64 v1, v2, v1, s[58:59]
	v_add_u32_e32 v3, s88, v1
.LBB0_485:
	s_sub_i32 s1, s36, s14
	s_ashr_i32 s15, s14, 31
	s_mul_i32 s64, s14, 0x1800
	s_mul_hi_i32 s37, s14, 0x1800
	s_add_u32 s64, s64, s80
	s_addc_u32 s65, s37, s81
	s_lshl_b64 vcc, s[14:15], 10
	s_add_u32 s94, vcc_lo, s78
	s_addc_u32 s95, vcc_hi, s79
	v_readfirstlane_b32 s0, v3
	v_lshl_add_u64 v[2:3], s[64:65], 0, v[78:79]
	s_ashr_i32 s37, s36, 31
	s_mul_i32 s64, s36, 0x1800
	s_mul_hi_i32 s15, s36, 0x1800
	s_add_u32 s64, s64, s80
	s_addc_u32 s65, s15, s81
	s_lshl_b64 s[36:37], s[36:37], 10
	s_add_u32 s36, s36, s78
	global_load_ushort v115, v[2:3], off
	global_load_ushort v116, v[2:3], off offset:512
	v_lshl_add_u64 v[2:3], s[94:95], 0, v[80:81]
	s_addc_u32 s37, s37, s79
	s_lshl_b32 s15, s1, 1
	global_load_ushort v117, v[2:3], off
	s_add_i32 s14, s15, s14
	v_lshl_add_u64 v[2:3], s[64:65], 0, v[78:79]
	global_load_ushort v118, v[2:3], off
	global_load_ushort v119, v[2:3], off offset:512
	v_lshl_add_u64 v[2:3], s[36:37], 0, v[80:81]
	s_ashr_i32 s15, s14, 31
	s_mul_i32 s36, s14, 0x1800
	s_mul_hi_i32 s37, s14, 0x1800
	s_add_u32 s36, s36, s80
	s_addc_u32 s37, s37, s81
	s_lshl_b64 s[64:65], s[14:15], 10
	s_add_u32 s64, s64, s78
	s_addc_u32 s65, s65, s79
	global_load_ushort v120, v[2:3], off
	s_add_i32 s14, s14, s1
	v_lshl_add_u64 v[2:3], s[36:37], 0, v[78:79]
	s_ashr_i32 s15, s14, 31
	s_mul_i32 s36, s14, 0x1800
	s_mul_hi_i32 s37, s14, 0x1800
	s_add_u32 s36, s36, s80
	global_load_ushort v121, v[2:3], off
	global_load_ushort v122, v[2:3], off offset:512
	v_lshl_add_u64 v[2:3], s[64:65], 0, v[80:81]
	s_addc_u32 s37, s37, s81
	s_lshl_b64 s[64:65], s[14:15], 10
	s_add_u32 s64, s64, s78
	s_addc_u32 s65, s65, s79
	global_load_ushort v123, v[2:3], off
	s_add_i32 s14, s14, s1
	v_lshl_add_u64 v[2:3], s[36:37], 0, v[78:79]
	s_ashr_i32 s15, s14, 31
	s_mul_i32 s36, s14, 0x1800
	s_mul_hi_i32 s37, s14, 0x1800
	s_add_u32 s36, s36, s80
	global_load_ushort v124, v[2:3], off
	global_load_ushort v125, v[2:3], off offset:512
	v_lshl_add_u64 v[2:3], s[64:65], 0, v[80:81]
	s_addc_u32 s37, s37, s81
	s_lshl_b64 s[64:65], s[14:15], 10
	s_add_u32 s64, s64, s78
	s_addc_u32 s65, s65, s79
	global_load_ushort v128, v[2:3], off
	s_add_i32 s14, s14, s1
	v_lshl_add_u64 v[2:3], s[36:37], 0, v[78:79]
	s_ashr_i32 s15, s14, 31
	s_mul_i32 s36, s14, 0x1800
	s_mul_hi_i32 s37, s14, 0x1800
	s_add_u32 s36, s36, s80
	global_load_ushort v129, v[2:3], off
	global_load_ushort v130, v[2:3], off offset:512
	v_lshl_add_u64 v[2:3], s[64:65], 0, v[80:81]
	s_addc_u32 s37, s37, s81
	s_lshl_b64 s[64:65], s[14:15], 10
	s_add_u32 s64, s64, s78
	s_addc_u32 s65, s65, s79
	global_load_ushort v131, v[2:3], off
	s_add_i32 s14, s14, s1
	v_lshl_add_u64 v[2:3], s[36:37], 0, v[78:79]
	s_ashr_i32 s15, s14, 31
	s_mul_i32 s36, s14, 0x1800
	s_mul_hi_i32 s37, s14, 0x1800
	s_add_u32 s36, s36, s80
	global_load_ushort v132, v[2:3], off
	global_load_ushort v133, v[2:3], off offset:512
	v_lshl_add_u64 v[2:3], s[64:65], 0, v[80:81]
	s_addc_u32 s37, s37, s81
	s_lshl_b64 s[64:65], s[14:15], 10
	s_add_u32 s64, s64, s78
	s_addc_u32 s65, s65, s79
	global_load_ushort v134, v[2:3], off
	s_add_i32 s14, s14, s1
	v_lshl_add_u64 v[2:3], s[36:37], 0, v[78:79]
	s_ashr_i32 s15, s14, 31
	s_mul_i32 s36, s14, 0x1800
	s_mul_hi_i32 s1, s14, 0x1800
	s_add_u32 s36, s36, s80
	s_addc_u32 s37, s1, s81
	s_lshl_b64 s[14:15], s[14:15], 10
	s_add_u32 s14, s14, s78
	global_load_ushort v135, v[2:3], off
	global_load_ushort v136, v[2:3], off offset:512
	v_lshl_add_u64 v[2:3], s[64:65], 0, v[80:81]
	s_addc_u32 s15, s15, s79
	global_load_ushort v137, v[2:3], off
	s_mul_hi_i32 s1, s93, 0x1800
	v_lshl_add_u64 v[2:3], s[36:37], 0, v[78:79]
	global_load_ushort v138, v[2:3], off
	global_load_ushort v139, v[2:3], off offset:512
	v_lshl_add_u64 v[2:3], s[14:15], 0, v[80:81]
	s_sub_i32 s36, s0, s93
	s_mul_i32 s14, s93, 0x1800
	s_add_u32 s14, s14, s80
	s_addc_u32 s15, s1, s81
	s_mul_hi_i32 s1, s0, 0x1800
	s_mulk_i32 s0, 0x1800
	s_add_u32 s0, s0, s80
	global_load_ushort v140, v[2:3], off
	s_addc_u32 s1, s1, s81
	v_lshl_add_u64 v[2:3], s[14:15], 0, v[82:83]
	global_load_ushort v2, v[2:3], off
	s_nop 0
	v_lshl_add_u64 v[4:5], s[0:1], 0, v[82:83]
	s_lshl_b32 s0, s36, 1
	s_add_i32 s14, s0, s93
	s_mul_i32 s0, s14, 0x1800
	s_mul_hi_i32 s1, s14, 0x1800
	s_add_u32 s0, s0, s80
	s_addc_u32 s1, s1, s81
	global_load_ushort v1, v[4:5], off
	s_add_i32 s14, s14, s36
	v_lshl_add_u64 v[4:5], s[0:1], 0, v[82:83]
	s_mul_i32 s0, s14, 0x1800
	s_mul_hi_i32 s1, s14, 0x1800
	s_add_u32 s0, s0, s80
	s_addc_u32 s1, s1, s81
	global_load_ushort v4, v[4:5], off
	s_add_i32 s14, s14, s36
	v_lshl_add_u64 v[6:7], s[0:1], 0, v[82:83]
	s_mul_i32 s0, s14, 0x1800
	s_mul_hi_i32 s1, s14, 0x1800
	s_add_u32 s0, s0, s80
	s_addc_u32 s1, s1, s81
	global_load_ushort v3, v[6:7], off
	s_add_i32 s14, s14, s36
	v_lshl_add_u64 v[6:7], s[0:1], 0, v[82:83]
	s_mul_i32 s0, s14, 0x1800
	s_mul_hi_i32 s1, s14, 0x1800
	s_add_u32 s0, s0, s80
	s_addc_u32 s1, s1, s81
	global_load_ushort v6, v[6:7], off
	s_add_i32 s14, s14, s36
	v_lshl_add_u64 v[8:9], s[0:1], 0, v[82:83]
	s_mul_i32 s0, s14, 0x1800
	s_mul_hi_i32 s1, s14, 0x1800
	s_add_u32 s0, s0, s80
	s_addc_u32 s1, s1, s81
	global_load_ushort v5, v[8:9], off
	s_add_i32 s14, s14, s36
	v_lshl_add_u64 v[8:9], s[0:1], 0, v[82:83]
	s_mul_i32 s0, s14, 0x1800
	s_mul_hi_i32 s1, s14, 0x1800
	s_add_u32 s0, s0, s80
	s_addc_u32 s1, s1, s81
	global_load_ushort v8, v[8:9], off
	s_add_i32 s14, s14, s36
	v_lshl_add_u64 v[10:11], s[0:1], 0, v[82:83]
	s_mul_i32 s0, s14, 0x1800
	s_mul_hi_i32 s1, s14, 0x1800
	s_add_u32 s0, s0, s80
	s_addc_u32 s1, s1, s81
	global_load_ushort v7, v[10:11], off
	s_add_i32 s14, s14, s36
	v_lshl_add_u64 v[10:11], s[0:1], 0, v[82:83]
	s_mul_i32 s0, s14, 0x1800
	s_mul_hi_i32 s1, s14, 0x1800
	s_add_u32 s0, s0, s80
	s_addc_u32 s1, s1, s81
	global_load_ushort v10, v[10:11], off
	s_add_i32 s14, s14, s36
	v_lshl_add_u64 v[12:13], s[0:1], 0, v[82:83]
	s_mul_i32 s0, s14, 0x1800
	s_mul_hi_i32 s1, s14, 0x1800
	s_add_u32 s0, s0, s80
	s_addc_u32 s1, s1, s81
	global_load_ushort v9, v[12:13], off
	s_add_i32 s14, s14, s36
	v_lshl_add_u64 v[12:13], s[0:1], 0, v[82:83]
	s_mul_i32 s0, s14, 0x1800
	s_mul_hi_i32 s1, s14, 0x1800
	s_add_u32 s0, s0, s80
	s_addc_u32 s1, s1, s81
	global_load_ushort v12, v[12:13], off
	s_add_i32 s14, s14, s36
	v_lshl_add_u64 v[14:15], s[0:1], 0, v[82:83]
	s_mul_i32 s0, s14, 0x1800
	s_mul_hi_i32 s1, s14, 0x1800
	s_add_u32 s0, s0, s80
	s_addc_u32 s1, s1, s81
	global_load_ushort v11, v[14:15], off
	s_add_i32 s14, s14, s36
	v_lshl_add_u64 v[14:15], s[0:1], 0, v[82:83]
	s_mul_i32 s0, s14, 0x1800
	s_mul_hi_i32 s1, s14, 0x1800
	s_add_u32 s0, s0, s80
	s_addc_u32 s1, s1, s81
	global_load_ushort v14, v[14:15], off
	s_add_i32 s14, s14, s36
	v_lshl_add_u64 v[30:31], s[0:1], 0, v[82:83]
	s_mul_i32 s0, s14, 0x1800
	s_mul_hi_i32 s1, s14, 0x1800
	s_add_u32 s0, s0, s80
	s_addc_u32 s1, s1, s81
	s_add_i32 s14, s14, s36
	s_mul_hi_i32 s15, s14, 0x1800
	s_mulk_i32 s14, 0x1800
	s_add_u32 s14, s14, s80
	global_load_ushort v13, v[30:31], off
	s_addc_u32 s15, s15, s81
	v_lshl_add_u64 v[30:31], s[0:1], 0, v[82:83]
	global_load_ushort v16, v[30:31], off
	s_nop 0
	v_lshl_add_u64 v[30:31], s[14:15], 0, v[82:83]
	global_load_ushort v15, v[30:31], off

.LBB0_488:
	s_andn2_b64 vcc, exec, s[0:1]
	s_cbranch_vccnz .LBB0_468
	v_add_u32_e32 v30, 0xff, v32
	v_cndmask_b32_e64 v30, v30, v31, s[58:59]
	v_add_u32_e32 v30, s88, v30
	s_branch .LBB0_468
.LBB0_490:
	s_add_i32 s14, s82, s91
	s_add_i32 s36, s14, 0xffffff40
	s_add_i32 s14, s16, s89
	s_add_i32 s37, s14, 0x8bf
	s_and_b64 s[14:15], s[58:59], exec
	s_cselect_b32 s36, s36, s37
	s_lshl_b32 s14, s36, 6
	s_and_b32 s14, s14, 0x7c0
	s_ashr_i32 s15, s36, 5
	s_add_i32 s37, s14, s15
	s_and_b64 s[14:15], s[38:39], exec
	s_cselect_b32 s14, s36, s37
	s_add_i32 s14, s14, s90
	s_cbranch_execnz .LBB0_474

.LBB0_492:
	s_add_i32 s15, s82, s91
	s_add_i32 s36, s16, s89
	s_addk_i32 s15, 0xff41
	s_add_i32 s64, s36, 0x8be
	s_and_b64 s[36:37], s[58:59], exec
	s_cselect_b32 s15, s15, s64
	s_lshl_b32 s36, s15, 6
	s_and_b32 s36, s36, 0x7c0
	s_ashr_i32 s37, s15, 5
	s_add_i32 s64, s36, s37
	s_and_b64 s[36:37], s[38:39], exec
	s_cselect_b32 s15, s15, s64
	s_add_i32 s36, s15, s90
	s_cbranch_execz .LBB0_476
	s_branch .LBB0_477
.LBB0_493:
	s_waitcnt lgkmcnt(0)
	s_add_u32 s42, s76, 0x15e00000
	s_addc_u32 s43, s77, 0
	s_lshl_b64 s[0:1], s[28:29], 3
	v_readlane_b32 s2, v254, 4
	v_readlane_b32 s3, v254, 5
	s_add_u32 s0, s2, s0
	s_addc_u32 s1, s3, s1
	s_waitcnt vmcnt(0)
	s_barrier
	s_load_dwordx4 s[44:47], s[0:1], 0x80
	s_cmpk_lt_i32 s20, 0x480
	s_cselect_b64 s[2:3], -1, 0
	s_cmpk_gt_i32 s20, 0x47f
	v_lshlrev_b32_e32 v148, 3, v127
	s_movk_i32 s93, 0x800
	v_readlane_b32 s82, v255, 43
	s_cbranch_scc1 .LBB0_554
	s_cmpk_gt_i32 s20, 0x3ff
	s_cselect_b64 s[0:1], -1, 0
	s_add_i32 s14, s20, 0xfffffc00
	s_cmpk_lt_i32 s20, 0x400
	s_cselect_b32 s16, s93, 0x100
	s_cselect_b32 s14, s20, s14
	s_lshr_b32 s15, s16, 6
	s_abs_i32 s17, s15
	v_cvt_f32_u32_e32 v1, s17
	s_sub_i32 s36, 0, s17
	s_abs_i32 s18, s14
	s_xor_b32 s19, s14, s15
	v_rcp_iflag_f32_e32 v1, v1
	s_ashr_i32 s19, s19, 31
	v_mov_b32_e32 v5, 0
	v_mov_b32_e32 v4, v5
	v_mul_f32_e32 v1, 0x4f7ffffe, v1
	v_cvt_u32_f32_e32 v1, v1
	v_mov_b32_e32 v3, v5
	v_mov_b32_e32 v2, v5
	v_readfirstlane_b32 s37, v1
	s_mul_i32 s36, s36, s37
	s_mul_hi_u32 s36, s37, s36
	s_add_i32 s37, s37, s36
	s_mul_hi_u32 s36, s18, s37
	s_mul_i32 s37, s36, s17
	s_sub_i32 s18, s18, s37
	s_add_i32 s40, s36, 1
	s_sub_i32 s37, s18, s17
	s_cmp_ge_u32 s18, s17
	s_cselect_b32 s36, s40, s36
	s_cselect_b32 s18, s37, s18
	s_add_i32 s37, s36, 1
	s_cmp_ge_u32 s18, s17
	s_cselect_b32 s17, s37, s36
	s_xor_b32 s17, s17, s19
	s_sub_i32 s17, s17, s19
	s_mul_i32 s15, s17, s15
	s_sub_i32 s14, s14, s15
	s_lshl_b32 s19, s14, 6
	s_lshl_b32 s14, s71, 3
	s_lshl_b32 s18, s17, 8
	s_lshl_b32 s17, s17, 11
	s_add_i32 s19, s19, s14
	s_addk_i32 s17, 0x2000
	s_add_i32 s36, s19, -1
	s_cmp_ge_u32 s36, s16
	s_cbranch_scc1 .LBB0_500
	s_mov_b64 s[14:15], -1
	s_and_b64 vcc, exec, s[0:1]
	s_cbranch_vccz .LBB0_497
	s_add_i32 s37, s36, s18
	s_mov_b64 s[14:15], 0

.LBB0_766:
	v_readlane_b32 s0, v254, 57
	v_readlane_b32 s1, v254, 58
	v_cvt_f32_u32_e32 v1, v3
	v_sub_u32_e32 v5, 0, v3
	v_rcp_iflag_f32_e32 v1, v1
	s_nop 1
	global_atomic_add v4, v34, v235, s[0:1] sc0
	buffer_inv sc1
	v_mul_f32_e32 v1, 0x4f7ffffe, v1
	v_cvt_u32_f32_e32 v1, v1
	v_mul_lo_u32 v5, v5, v1
	v_mul_hi_u32 v5, v1, v5
	v_add_u32_e32 v1, v1, v5
	s_waitcnt vmcnt(0)
	v_mul_hi_u32 v1, v4, v1
	v_mul_lo_u32 v5, v1, v3
	v_sub_u32_e32 v5, v4, v5
	v_add_u32_e32 v6, 1, v1
	v_cmp_ge_u32_e32 vcc, v5, v3
	v_add_u32_e32 v4, 1, v4
	s_nop 0
	v_cndmask_b32_e32 v1, v1, v6, vcc
	v_sub_u32_e32 v6, v5, v3
	v_cndmask_b32_e32 v5, v5, v6, vcc
	v_add_u32_e32 v6, 1, v1
	v_cmp_ge_u32_e32 vcc, v5, v3
	s_nop 1
	v_cndmask_b32_e32 v1, v1, v6, vcc
	v_mul_lo_u32 v5, v3, v1
	v_add_u32_e32 v3, v5, v3
	v_cmp_ne_u32_e32 vcc, v4, v3
	s_and_saveexec_b64 s[0:1], vcc
	s_xor_b64 s[0:1], exec, s[0:1]
	s_cbranch_execz .LBB0_780
	v_readlane_b32 s14, v254, 59
	v_readlane_b32 s15, v254, 60
	s_waitcnt lgkmcnt(0)
	s_nop 3
	global_load_dword v2, v34, s[14:15] sc1
	s_waitcnt vmcnt(0)
	v_cmp_eq_u32_e32 vcc, v2, v1
	s_and_saveexec_b64 s[14:15], vcc
	s_cbranch_execz .LBB0_779
	s_mov_b32 s17, 1
	s_mov_b64 s[18:19], 0
	s_branch .LBB0_770

.LBB0_1180:
	v_readlane_b32 s0, v254, 57
	v_readlane_b32 s1, v254, 58
	v_cvt_f32_u32_e32 v1, v3
	v_sub_u32_e32 v5, 0, v3
	v_rcp_iflag_f32_e32 v1, v1
	s_nop 1
	global_atomic_add v4, v34, v235, s[0:1] sc0
	buffer_inv sc1
	v_mul_f32_e32 v1, 0x4f7ffffe, v1
	v_cvt_u32_f32_e32 v1, v1
	v_mul_lo_u32 v5, v5, v1
	v_mul_hi_u32 v5, v1, v5
	v_add_u32_e32 v1, v1, v5
	s_waitcnt vmcnt(0)
	v_mul_hi_u32 v1, v4, v1
	v_mul_lo_u32 v5, v1, v3
	v_sub_u32_e32 v5, v4, v5
	v_add_u32_e32 v6, 1, v1
	v_cmp_ge_u32_e32 vcc, v5, v3
	v_add_u32_e32 v4, 1, v4
	s_nop 0
	v_cndmask_b32_e32 v1, v1, v6, vcc
	v_sub_u32_e32 v6, v5, v3
	v_cndmask_b32_e32 v5, v5, v6, vcc
	v_add_u32_e32 v6, 1, v1
	v_cmp_ge_u32_e32 vcc, v5, v3
	s_nop 1
	v_cndmask_b32_e32 v1, v1, v6, vcc
	v_mul_lo_u32 v5, v3, v1
	v_add_u32_e32 v3, v5, v3
	v_cmp_ne_u32_e32 vcc, v4, v3
	s_and_saveexec_b64 s[0:1], vcc
	s_xor_b64 s[0:1], exec, s[0:1]
	s_cbranch_execz .LBB0_1194
	v_readlane_b32 s14, v254, 59
	v_readlane_b32 s15, v254, 60
	s_waitcnt lgkmcnt(0)
	s_nop 3
	global_load_dword v2, v34, s[14:15] sc1
	s_waitcnt vmcnt(0)
	v_cmp_eq_u32_e32 vcc, v2, v1
	s_and_saveexec_b64 s[14:15], vcc
	s_cbranch_execz .LBB0_1193
	s_mov_b32 s13, 1
	s_mov_b64 s[16:17], 0
	s_branch .LBB0_1184

.LBB0_1273:
	v_readlane_b32 s0, v254, 57
	v_readlane_b32 s1, v254, 58
	v_cvt_f32_u32_e32 v1, v3
	v_sub_u32_e32 v5, 0, v3
	v_rcp_iflag_f32_e32 v1, v1
	s_nop 1
	global_atomic_add v4, v34, v235, s[0:1] sc0
	buffer_inv sc1
	v_mul_f32_e32 v1, 0x4f7ffffe, v1
	v_cvt_u32_f32_e32 v1, v1
	v_mul_lo_u32 v5, v5, v1
	v_mul_hi_u32 v5, v1, v5
	v_add_u32_e32 v1, v1, v5
	s_waitcnt vmcnt(0)
	v_mul_hi_u32 v1, v4, v1
	v_mul_lo_u32 v5, v1, v3
	v_sub_u32_e32 v5, v4, v5
	v_add_u32_e32 v6, 1, v1
	v_cmp_ge_u32_e32 vcc, v5, v3
	v_add_u32_e32 v4, 1, v4
	s_nop 0
	v_cndmask_b32_e32 v1, v1, v6, vcc
	v_sub_u32_e32 v6, v5, v3
	v_cndmask_b32_e32 v5, v5, v6, vcc
	v_add_u32_e32 v6, 1, v1
	v_cmp_ge_u32_e32 vcc, v5, v3
	s_nop 1
	v_cndmask_b32_e32 v1, v1, v6, vcc
	v_mul_lo_u32 v5, v3, v1
	v_add_u32_e32 v3, v5, v3
	v_cmp_ne_u32_e32 vcc, v4, v3
	s_and_saveexec_b64 s[0:1], vcc
	s_xor_b64 s[0:1], exec, s[0:1]
	s_cbranch_execz .LBB0_1287
	v_readlane_b32 s14, v254, 59
	v_readlane_b32 s15, v254, 60
	s_waitcnt lgkmcnt(0)
	s_nop 3
	global_load_dword v2, v34, s[14:15] sc1
	s_waitcnt vmcnt(0)
	v_cmp_eq_u32_e32 vcc, v2, v1
	s_and_saveexec_b64 s[14:15], vcc
	s_cbranch_execz .LBB0_1286
	s_mov_b32 s20, 1
	s_mov_b64 s[16:17], 0
	s_branch .LBB0_1277

.LBB0_1391:
	global_atomic_add v[2:3], v235, off
	v_add_co_u32_e32 v2, vcc, 0xffffef00, v2
	s_nop 1
	v_addc_co_u32_e32 v3, vcc, -1, v3, vcc
	global_atomic_add v[2:3], v235, off
	global_atomic_add v[2:3], v235, off offset:256
	global_atomic_add v[2:3], v235, off offset:512
	global_atomic_add v[2:3], v235, off offset:768
	global_atomic_add v[2:3], v235, off offset:1024
	global_atomic_add v[2:3], v235, off offset:1280
	global_atomic_add v[2:3], v235, off offset:1536
	global_atomic_add v[2:3], v235, off offset:1792
	global_atomic_add v[2:3], v235, off offset:2048
	global_atomic_add v[2:3], v235, off offset:2304
	global_atomic_add v[2:3], v235, off offset:2560
	global_atomic_add v[2:3], v235, off offset:2816
	global_atomic_add v[2:3], v235, off offset:3072
	global_atomic_add v[2:3], v235, off offset:3328
	global_atomic_add v[2:3], v235, off offset:3584
	global_atomic_add v[2:3], v235, off offset:3840
	s_getpc_b64 s[98:99]

	.amdhsa_kernel _Z10fwd_kernel4Args
		.amdhsa_group_segment_fixed_size 0
		.amdhsa_private_segment_fixed_size 0
		.amdhsa_kernarg_size 576
		.amdhsa_user_sgpr_count 2
		.amdhsa_user_sgpr_dispatch_ptr 0
		.amdhsa_user_sgpr_queue_ptr 0
		.amdhsa_user_sgpr_kernarg_segment_ptr 1
		.amdhsa_user_sgpr_dispatch_id 0
		.amdhsa_user_sgpr_kernarg_preload_length 0
		.amdhsa_user_sgpr_kernarg_preload_offset 0
		.amdhsa_user_sgpr_private_segment_size 0
		.amdhsa_uses_dynamic_stack 0
		.amdhsa_enable_private_segment 0
		.amdhsa_system_sgpr_workgroup_id_x 1
		.amdhsa_system_sgpr_workgroup_id_y 0
		.amdhsa_system_sgpr_workgroup_id_z 0
		.amdhsa_system_sgpr_workgroup_info 0
		.amdhsa_system_vgpr_workitem_id 0
		.amdhsa_next_free_vgpr 256
		.amdhsa_next_free_sgpr 100
		.amdhsa_accum_offset 256
		.amdhsa_reserve_vcc 1
		.amdhsa_float_round_mode_32 0
		.amdhsa_float_round_mode_16_64 0
		.amdhsa_float_denorm_mode_32 3
		.amdhsa_float_denorm_mode_16_64 3
		.amdhsa_dx10_clamp 1
		.amdhsa_ieee_mode 1
		.amdhsa_fp16_overflow 0
		.amdhsa_tg_split 0
		.amdhsa_exception_fp_ieee_invalid_op 0
		.amdhsa_exception_fp_denorm_src 0
		.amdhsa_exception_fp_ieee_div_zero 0
		.amdhsa_exception_fp_ieee_overflow 0
		.amdhsa_exception_fp_ieee_underflow 0
		.amdhsa_exception_fp_ieee_inexact 0
		.amdhsa_exception_int_div_zero 0
	.end_amdhsa_kernel

amdhsa.kernels:
  - .agpr_count:     0
    .args:
      - .offset:         0
        .size:           320
        .value_kind:     by_value
      - .offset:         320
        .size:           4
        .value_kind:     hidden_block_count_x
      - .offset:         324
        .size:           4
        .value_kind:     hidden_block_count_y
      - .offset:         328
        .size:           4
        .value_kind:     hidden_block_count_z
      - .offset:         332
        .size:           2
        .value_kind:     hidden_group_size_x
      - .offset:         334
        .size:           2
        .value_kind:     hidden_group_size_y
      - .offset:         336
        .size:           2
        .value_kind:     hidden_group_size_z
      - .offset:         338
        .size:           2
        .value_kind:     hidden_remainder_x
      - .offset:         340
        .size:           2
        .value_kind:     hidden_remainder_y
      - .offset:         342
        .size:           2
        .value_kind:     hidden_remainder_z
      - .offset:         360
        .size:           8
        .value_kind:     hidden_global_offset_x
      - .offset:         368
        .size:           8
        .value_kind:     hidden_global_offset_y
      - .offset:         376
        .size:           8
        .value_kind:     hidden_global_offset_z
      - .offset:         384
        .size:           2
        .value_kind:     hidden_grid_dims
      - .offset:         440
        .size:           4
        .value_kind:     hidden_dynamic_lds_size
    .group_segment_fixed_size: 0
    .kernarg_segment_align: 8
    .kernarg_segment_size: 576
    .language:       OpenCL C
    .language_version:
      - 2
      - 0
    .max_flat_workgroup_size: 512
    .name:           _Z10fwd_kernel4Args
    .private_segment_fixed_size: 0
    .sgpr_count:     106
    .sgpr_spill_count: 112
    .symbol:         _Z10fwd_kernel4Args.kd
    .uniform_work_group_size: 1
    .uses_dynamic_stack: false
    .vgpr_count:     256
    .vgpr_spill_count: 0
    .wavefront_size: 64
